# v17 + s_setprio removed from the phase-2/6 GEMM k-loops
# speedup vs baseline: 1.0248x; 1.0072x over previous
.LBB0_210:
	s_barrier
	s_waitcnt lgkmcnt(7)
	v_mfma_f32_16x16x32_bf16 v[122:125], v[130:133], v[174:177], v[122:125]
	v_mfma_f32_16x16x32_bf16 v[126:129], v[134:137], v[174:177], v[126:129]
	v_mfma_f32_16x16x32_bf16 v[114:117], v[138:141], v[174:177], v[114:117]
	v_mfma_f32_16x16x32_bf16 v[110:113], v[142:145], v[174:177], v[110:113]
	s_waitcnt lgkmcnt(6)
	v_mfma_f32_16x16x32_bf16 v[106:109], v[130:133], v[170:173], v[106:109]
	v_mfma_f32_16x16x32_bf16 v[118:121], v[134:137], v[170:173], v[118:121]
	v_mfma_f32_16x16x32_bf16 v[98:101], v[138:141], v[170:173], v[98:101]
	v_mfma_f32_16x16x32_bf16 v[94:97], v[142:145], v[170:173], v[94:97]
	s_waitcnt lgkmcnt(5)
	v_mfma_f32_16x16x32_bf16 v[90:93], v[130:133], v[166:169], v[90:93]
	v_mfma_f32_16x16x32_bf16 v[102:105], v[134:137], v[166:169], v[102:105]
	v_mfma_f32_16x16x32_bf16 v[82:85], v[138:141], v[166:169], v[82:85]
	v_mfma_f32_16x16x32_bf16 v[78:81], v[142:145], v[166:169], v[78:81]
	s_waitcnt lgkmcnt(4)
	v_mfma_f32_16x16x32_bf16 v[74:77], v[130:133], v[162:165], v[74:77]
	v_mfma_f32_16x16x32_bf16 v[86:89], v[134:137], v[162:165], v[86:89]
	v_mfma_f32_16x16x32_bf16 v[70:73], v[138:141], v[162:165], v[70:73]
	v_mfma_f32_16x16x32_bf16 v[62:65], v[142:145], v[162:165], v[62:65]
	s_waitcnt lgkmcnt(3)
	v_mfma_f32_16x16x32_bf16 v[58:61], v[130:133], v[158:161], v[58:61]
	v_mfma_f32_16x16x32_bf16 v[66:69], v[134:137], v[158:161], v[66:69]
	v_mfma_f32_16x16x32_bf16 v[54:57], v[138:141], v[158:161], v[54:57]
	v_mfma_f32_16x16x32_bf16 v[46:49], v[142:145], v[158:161], v[46:49]
	s_waitcnt lgkmcnt(2)
	v_mfma_f32_16x16x32_bf16 v[42:45], v[130:133], v[154:157], v[42:45]
	v_mfma_f32_16x16x32_bf16 v[50:53], v[134:137], v[154:157], v[50:53]
	v_mfma_f32_16x16x32_bf16 v[38:41], v[138:141], v[154:157], v[38:41]
	v_mfma_f32_16x16x32_bf16 v[34:37], v[142:145], v[154:157], v[34:37]
	s_waitcnt lgkmcnt(1)
	v_mfma_f32_16x16x32_bf16 v[26:29], v[130:133], v[150:153], v[26:29]
	v_mfma_f32_16x16x32_bf16 v[30:33], v[134:137], v[150:153], v[30:33]
	v_mfma_f32_16x16x32_bf16 v[22:25], v[138:141], v[150:153], v[22:25]
	v_mfma_f32_16x16x32_bf16 v[18:21], v[142:145], v[150:153], v[18:21]
	s_waitcnt lgkmcnt(0)
	v_mfma_f32_16x16x32_bf16 v[10:13], v[130:133], v[146:149], v[10:13]
	v_mfma_f32_16x16x32_bf16 v[14:17], v[134:137], v[146:149], v[14:17]
	v_mfma_f32_16x16x32_bf16 v[6:9], v[138:141], v[146:149], v[6:9]
	v_mfma_f32_16x16x32_bf16 v[2:5], v[142:145], v[146:149], v[2:5]
	s_add_i32 s2, s86, 1
	s_cmp_lg_u32 s86, 2
	s_cselect_b32 s86, s2, 0
	s_add_i32 s2, s84, 1
	s_barrier
	s_cmp_lg_u32 s84, 2
	s_cselect_b32 s84, s2, 0
	s_add_i32 s85, s85, 1
	v_lshl_add_u64 v[180:181], v[180:181], 0, 64
	v_lshl_add_u64 v[182:183], v[182:183], 0, 64
	v_lshl_add_u64 v[184:185], v[184:185], 0, s[40:41]
	s_cmp_eq_u32 s85, 64
	v_lshl_add_u64 v[186:187], v[186:187], 0, s[40:41]
	s_cbranch_scc1 .LBB0_217

.LBB0_614:
	s_barrier
	s_waitcnt lgkmcnt(7)
	v_mfma_f32_16x16x32_bf16 v[126:129], v[130:133], v[174:177], v[126:129]
	v_mfma_f32_16x16x32_bf16 v[102:105], v[134:137], v[174:177], v[102:105]
	v_mfma_f32_16x16x32_bf16 v[70:73], v[138:141], v[174:177], v[70:73]
	v_mfma_f32_16x16x32_bf16 v[38:41], v[142:145], v[174:177], v[38:41]
	s_waitcnt lgkmcnt(6)
	v_mfma_f32_16x16x32_bf16 v[122:125], v[130:133], v[170:173], v[122:125]
	v_mfma_f32_16x16x32_bf16 v[94:97], v[134:137], v[170:173], v[94:97]
	v_mfma_f32_16x16x32_bf16 v[62:65], v[138:141], v[170:173], v[62:65]
	v_mfma_f32_16x16x32_bf16 v[30:33], v[142:145], v[170:173], v[30:33]
	s_waitcnt lgkmcnt(5)
	v_mfma_f32_16x16x32_bf16 v[118:121], v[130:133], v[166:169], v[118:121]
	v_mfma_f32_16x16x32_bf16 v[86:89], v[134:137], v[166:169], v[86:89]
	v_mfma_f32_16x16x32_bf16 v[54:57], v[138:141], v[166:169], v[54:57]
	v_mfma_f32_16x16x32_bf16 v[22:25], v[142:145], v[166:169], v[22:25]
	s_waitcnt lgkmcnt(4)
	v_mfma_f32_16x16x32_bf16 v[114:117], v[130:133], v[162:165], v[114:117]
	v_mfma_f32_16x16x32_bf16 v[82:85], v[134:137], v[162:165], v[82:85]
	v_mfma_f32_16x16x32_bf16 v[50:53], v[138:141], v[162:165], v[50:53]
	v_mfma_f32_16x16x32_bf16 v[18:21], v[142:145], v[162:165], v[18:21]
	s_waitcnt lgkmcnt(3)
	v_mfma_f32_16x16x32_bf16 v[110:113], v[130:133], v[158:161], v[110:113]
	v_mfma_f32_16x16x32_bf16 v[78:81], v[134:137], v[158:161], v[78:81]
	v_mfma_f32_16x16x32_bf16 v[46:49], v[138:141], v[158:161], v[46:49]
	v_mfma_f32_16x16x32_bf16 v[14:17], v[142:145], v[158:161], v[14:17]
	s_waitcnt lgkmcnt(2)
	v_mfma_f32_16x16x32_bf16 v[106:109], v[130:133], v[154:157], v[106:109]
	v_mfma_f32_16x16x32_bf16 v[74:77], v[134:137], v[154:157], v[74:77]
	v_mfma_f32_16x16x32_bf16 v[42:45], v[138:141], v[154:157], v[42:45]
	v_mfma_f32_16x16x32_bf16 v[10:13], v[142:145], v[154:157], v[10:13]
	s_waitcnt lgkmcnt(1)
	v_mfma_f32_16x16x32_bf16 v[98:101], v[130:133], v[150:153], v[98:101]
	v_mfma_f32_16x16x32_bf16 v[66:69], v[134:137], v[150:153], v[66:69]
	v_mfma_f32_16x16x32_bf16 v[34:37], v[138:141], v[150:153], v[34:37]
	v_mfma_f32_16x16x32_bf16 v[6:9], v[142:145], v[150:153], v[6:9]
	s_waitcnt lgkmcnt(0)
	v_mfma_f32_16x16x32_bf16 v[90:93], v[130:133], v[146:149], v[90:93]
	v_mfma_f32_16x16x32_bf16 v[58:61], v[134:137], v[146:149], v[58:61]
	v_mfma_f32_16x16x32_bf16 v[26:29], v[138:141], v[146:149], v[26:29]
	v_mfma_f32_16x16x32_bf16 v[2:5], v[142:145], v[146:149], v[2:5]
	s_add_i32 s2, s62, 1
	s_cmp_lg_u32 s62, 2
	s_cselect_b32 s62, s2, 0
	s_add_i32 s2, s60, 1
	s_barrier
	s_cmp_lg_u32 s60, 2
	s_cselect_b32 s60, s2, 0
	s_add_i32 s61, s61, 1
	v_lshl_add_u64 v[180:181], v[180:181], 0, 64
	v_lshl_add_u64 v[182:183], v[182:183], 0, 64
	v_lshl_add_u64 v[184:185], v[184:185], 0, s[20:21]
	s_cmp_eq_u32 s61, 64
	v_lshl_add_u64 v[186:187], v[186:187], 0, s[20:21]
	s_cbranch_scc1 .LBB0_621
